# prep work queue: software-pipelined dequeue (next slot claimed under the current unit, published at the next loop top)
# baseline (speedup 1.0000x reference)
.LBB0_610:
	s_mov_b32 s65, s49
	s_load_dwordx2 s[52:53], s[92:93], 0x90
	s_lshl_b32 s48, s45, 14
	s_lshl_b64 s[4:5], s[48:49], 11
	s_movk_i32 s54, 0x400
	s_waitcnt lgkmcnt(0)
	s_add_u32 s4, s52, s4
	s_addc_u32 s5, s53, s5
	s_add_u32 s4, s4, 0x7100000
	v_writelane_b32 v255, s4, 32
	s_addc_u32 s81, s5, 0
	v_readlane_b32 s4, v255, 0
	s_add_u32 s10, s52, s4
	s_addc_u32 s11, s53, 0
	s_lshl_b64 s[4:5], s[48:49], 6
	s_add_u32 s4, s52, s4
	s_addc_u32 s5, s53, s5
	s_load_dwordx2 s[6:7], s[92:93], 0x18
	s_load_dwordx2 s[0:1], s[92:93], 0x30
	s_add_u32 s4, s4, 0xb100000
	s_addc_u32 s5, s5, 0
	v_writelane_b32 v255, s4, 48
	s_nop 1
	v_writelane_b32 v255, s5, 49
	s_nop 0
	v_readlane_b32 s4, v255, 3
	v_readlane_b32 s5, v255, 4
	s_waitcnt lgkmcnt(0)
	s_add_u32 s4, s6, s4
	s_addc_u32 s5, s7, s5
	v_readlane_b32 s6, v255, 9
	v_readlane_b32 s7, v255, 10
	s_add_u32 s58, s0, s6
	s_addc_u32 s59, s1, s7
	s_lshl_b32 s0, s45, 6
	v_readlane_b32 s6, v255, 1
	s_or_b32 s48, s0, s6
	s_lshl_b64 s[0:1], s[48:49], 2
	s_add_u32 s0, s52, s0
	s_addc_u32 s1, s53, s1
	s_add_u32 s60, s0, 0x10800
	s_addc_u32 s61, s1, 0
	s_add_i32 s80, s65, 0x1ffc0
	s_add_u32 s0, s52, 0xe400000
	s_addc_u32 s1, s53, 0
	v_readlane_b32 s7, v255, 2
	v_writelane_b32 v255, s0, 56
	s_nop 1
	v_writelane_b32 v255, s1, 57
	s_add_u32 s0, s52, 0x300000
	v_writelane_b32 v255, s0, 58
	s_addc_u32 s0, s53, 0
	s_add_u32 s85, s52, 0xd000000
	s_addc_u32 s88, s53, 0
	s_add_u32 s66, s52, 0x1e400000
	s_addc_u32 s67, s53, 0
	s_add_u32 s89, s52, 0x1e600000
	s_addc_u32 s94, s53, 0
	s_add_u32 s44, s52, 0xc400000
	s_addc_u32 s45, s53, 0
	s_add_u32 s91, s52, 0xd400000
	v_writelane_b32 v255, s0, 59
	s_addc_u32 s0, s53, 0
	v_writelane_b32 v255, s0, 50
	s_add_u32 s0, s52, 0x1e500000
	s_addc_u32 s1, s53, 0
	v_writelane_b32 v255, s0, 28
	s_add_u32 s96, s52, 0x200000
	s_addc_u32 s97, s53, 0
	v_writelane_b32 v255, s1, 29
	s_nop 0
	v_readlane_b32 s0, v255, 11
	s_add_u32 s0, s52, s0
	s_addc_u32 s1, s53, 0
	s_add_u32 s0, s0, 0x7000000
	v_writelane_b32 v255, s0, 54
	s_addc_u32 s0, s1, 0
	v_writelane_b32 v255, s0, 38
	s_add_u32 s0, s52, 0x1c800000
	v_writelane_b32 v255, s0, 36
	s_addc_u32 s0, s53, 0
	v_writelane_b32 v255, s0, 40
	s_nop 0
	v_readlane_b32 s0, v255, 12
	v_readlane_b32 s1, v255, 13
	s_add_u32 s0, s52, s0
	s_addc_u32 s1, s53, s1
	s_add_u32 s0, s0, 0x6f00000
	v_writelane_b32 v255, s0, 34
	s_addc_u32 s0, s1, 0
	v_writelane_b32 v255, s0, 42
	s_add_u32 s0, s52, 0x1bc00000
	v_writelane_b32 v255, s0, 60
	s_addc_u32 s0, s53, 0
	v_writelane_b32 v255, s0, 61
	s_add_i32 s0, s65, 0x21000
	v_writelane_b32 v255, s0, 30
	s_add_i32 s0, s65, 0x21400
	s_ashr_i32 s55, s54, 31
	v_writelane_b32 v255, s0, 25
	s_lshr_b32 s0, s55, 26
	s_add_i32 s0, s54, s0
	s_add_i32 s84, s65, 0x10000
	s_add_i32 s95, s65, 0x14000
	s_add_i32 s68, s65, 0x18000
	s_add_i32 s69, s65, 0x1c000
	s_ashr_i32 s46, s0, 6
	s_lshl_b64 s[82:83], s[54:55], 8
	s_lshl_b64 s[76:77], s[54:55], 9
	s_lshl_b64 s[0:1], s[54:55], 14
	s_add_u32 s0, s10, s0
	s_addc_u32 s1, s11, s1
	s_add_u32 s78, s0, 0x4600000
	s_addc_u32 s79, s1, 0
	s_add_u32 s0, s4, 0x3c00
	s_addc_u32 s1, s5, 0
	v_writelane_b32 v255, s0, 62
	s_cmp_gt_i32 s54, 63
	s_nop 0
	v_writelane_b32 v255, s1, 63
	s_cselect_b64 s[0:1], -1, 0
	v_writelane_b32 v255, s0, 26
	s_add_i32 s47, s46, -2
	s_nop 0
	v_writelane_b32 v255, s1, 27
	s_add_u32 s0, s52, 0x1b400000
	v_writelane_b32 v255, s0, 23
	s_addc_u32 s0, s53, 0
	v_writelane_b32 v255, s0, 44
	s_mov_b64 s[0:1], exec
	v_readlane_b32 s4, v254, 5
	v_readlane_b32 s5, v254, 6
	s_and_b64 s[4:5], s[0:1], s[4:5]
	s_mov_b64 exec, s[4:5]
	s_cbranch_execz .Lpq_e0
	v_mov_b32_e32 v252, 1
	global_atomic_add v252, v3, v252, s[60:61] sc0
.Lpq_e0:
	s_mov_b64 exec, s[0:1]
	s_branch .LBB0_614

.LBB0_614:
	s_mov_b64 s[6:7], exec
	v_readlane_b32 s4, v254, 5
	v_readlane_b32 s5, v254, 6
	s_and_b64 s[4:5], s[6:7], s[4:5]
	s_mov_b64 exec, s[4:5]
	s_waitcnt vmcnt(0)
	v_mov_b32_e32 v4, s80
	ds_write_b32 v4, v252
	s_mov_b64 exec, s[6:7]
	v_mov_b32_e32 v2, s80
	s_waitcnt vmcnt(0) lgkmcnt(0)
	s_barrier
	ds_read_b32 v2, v2
	s_movk_i32 s0, 0x37f
	s_waitcnt lgkmcnt(0)
	s_barrier
	s_mov_b64 exec, s[4:5]
	s_cbranch_execz .Lpq_e1
	v_mov_b32_e32 v252, 1
	global_atomic_add v252, v3, v252, s[60:61] sc0
.Lpq_e1:
	s_mov_b64 exec, s[6:7]
	v_cmp_lt_i32_e32 vcc, s0, v2
	v_readfirstlane_b32 s55, v2
	s_mov_b64 s[0:1], -1
	s_cbranch_vccnz .LBB0_613
	s_cmpk_gt_i32 s55, 0xff
	s_cbranch_scc0 .LBB0_689
	s_cmpk_gt_u32 s55, 0x13f
	s_cbranch_scc0 .LBB0_669
	s_cmpk_gt_u32 s55, 0x23f
	s_cbranch_scc0 .LBB0_662
	s_cmpk_gt_u32 s55, 0x33f
	s_cbranch_scc0 .LBB0_626
	v_mov_b32_e32 v65, v233
	s_lshl_b32 s0, s55, 8
	v_ashrrev_i32_e32 v2, 1, v65
	s_add_i32 s48, s0, 0xfffcc000
	v_and_b32_e32 v2, 0xffffffe0, v2
	v_add_u32_e32 v4, s48, v2
	v_ashrrev_i32_e32 v5, 31, v4
	v_readlane_b32 s0, v255, 56
	v_and_b32_e32 v64, 63, v65
	v_lshlrev_b64 v[4:5], 9, v[4:5]
	v_readlane_b32 s1, v255, 57
	v_lshlrev_b32_e32 v2, 3, v64
	s_nop 0
	v_lshl_add_u64 v[4:5], s[0:1], 0, v[4:5]
	v_lshl_add_u64 v[20:21], v[4:5], 0, v[2:3]
	global_load_dwordx2 v[66:67], v[20:21], off
	global_load_dwordx2 v[68:69], v[20:21], off offset:512
	global_load_dwordx2 v[62:63], v[20:21], off offset:1024
	global_load_dwordx2 v[60:61], v[20:21], off offset:1536
	global_load_dwordx2 v[54:55], v[20:21], off offset:2048
	global_load_dwordx2 v[50:51], v[20:21], off offset:2560
	global_load_dwordx2 v[44:45], v[20:21], off offset:3072
	global_load_dwordx2 v[42:43], v[20:21], off offset:3584
	s_movk_i32 s0, 0x1000
	v_add_co_u32_e32 v4, vcc, s0, v20
	s_movk_i32 s0, 0x2000
	s_nop 0
	v_addc_co_u32_e32 v5, vcc, 0, v21, vcc
	v_add_co_u32_e32 v24, vcc, s0, v20
	s_movk_i32 s0, 0x3000
	s_nop 0
	v_addc_co_u32_e32 v25, vcc, 0, v21, vcc
	global_load_dwordx2 v[56:57], v[24:25], off offset:-4096
	global_load_dwordx2 v[58:59], v[4:5], off offset:512
	global_load_dwordx2 v[52:53], v[4:5], off offset:1024
	global_load_dwordx2 v[48:49], v[4:5], off offset:1536
	global_load_dwordx2 v[46:47], v[4:5], off offset:2048
	global_load_dwordx2 v[30:31], v[4:5], off offset:2560
	global_load_dwordx2 v[26:27], v[4:5], off offset:3072
	global_load_dwordx2 v[22:23], v[4:5], off offset:3584
	global_load_dwordx2 v[18:19], v[24:25], off
	global_load_dwordx2 v[16:17], v[24:25], off offset:512
	global_load_dwordx2 v[14:15], v[24:25], off offset:1024
	global_load_dwordx2 v[12:13], v[24:25], off offset:1536
	global_load_dwordx2 v[10:11], v[24:25], off offset:2048
	global_load_dwordx2 v[8:9], v[24:25], off offset:2560
	global_load_dwordx2 v[6:7], v[24:25], off offset:3072
	global_load_dwordx2 v[4:5], v[24:25], off offset:3584
	v_add_co_u32_e32 v20, vcc, s0, v20
	v_lshl_add_u32 v2, v65, 4, s65
	s_nop 0
	v_addc_co_u32_e32 v21, vcc, 0, v21, vcc
	global_load_dwordx2 v[40:41], v[20:21], off
	global_load_dwordx2 v[38:39], v[20:21], off offset:512
	global_load_dwordx2 v[36:37], v[20:21], off offset:1024
	global_load_dwordx2 v[34:35], v[20:21], off offset:1536
	global_load_dwordx2 v[32:33], v[20:21], off offset:2048
	global_load_dwordx2 v[28:29], v[20:21], off offset:2560
	global_load_dwordx2 v[24:25], v[20:21], off offset:3072
	s_nop 0
	global_load_dwordx2 v[20:21], v[20:21], off offset:3584
	v_cmp_gt_u32_e32 vcc, 64, v65
	s_waitcnt vmcnt(31)
	v_lshlrev_b32_e32 v70, 16, v66
	v_and_b32_e32 v71, 0xffff0000, v66
	v_lshlrev_b32_e32 v66, 16, v67
	v_and_b32_e32 v67, 0xffff0000, v67
	s_waitcnt vmcnt(30)
	v_lshlrev_b32_e32 v72, 16, v68
	v_and_b32_e32 v73, 0xffff0000, v68
	v_lshlrev_b32_e32 v68, 16, v69
	v_and_b32_e32 v69, 0xffff0000, v69
	v_pk_add_f32 v[70:71], v[70:71], 0 op_sel_hi:[1,0]
	v_pk_add_f32 v[66:67], v[66:67], 0 op_sel_hi:[1,0]
	v_pk_add_f32 v[70:71], v[70:71], v[72:73]
	s_waitcnt vmcnt(29)
	v_lshlrev_b32_e32 v72, 16, v62
	v_and_b32_e32 v73, 0xffff0000, v62
	v_pk_add_f32 v[66:67], v[66:67], v[68:69]
	v_lshlrev_b32_e32 v62, 16, v63
	v_and_b32_e32 v63, 0xffff0000, v63
	v_pk_add_f32 v[70:71], v[70:71], v[72:73]
	s_waitcnt vmcnt(28)
	v_lshlrev_b32_e32 v72, 16, v60
	v_and_b32_e32 v73, 0xffff0000, v60
	v_pk_add_f32 v[62:63], v[66:67], v[62:63]
	v_lshlrev_b32_e32 v60, 16, v61
	v_and_b32_e32 v61, 0xffff0000, v61
	v_pk_add_f32 v[70:71], v[70:71], v[72:73]
	s_waitcnt vmcnt(27)
	v_lshlrev_b32_e32 v72, 16, v54
	v_and_b32_e32 v73, 0xffff0000, v54
	v_pk_add_f32 v[60:61], v[62:63], v[60:61]
	v_lshlrev_b32_e32 v54, 16, v55
	v_and_b32_e32 v55, 0xffff0000, v55
	v_pk_add_f32 v[70:71], v[70:71], v[72:73]
	s_waitcnt vmcnt(26)
	v_lshlrev_b32_e32 v72, 16, v50
	v_and_b32_e32 v73, 0xffff0000, v50
	v_pk_add_f32 v[54:55], v[60:61], v[54:55]
	v_lshlrev_b32_e32 v50, 16, v51
	v_and_b32_e32 v51, 0xffff0000, v51
	v_pk_add_f32 v[70:71], v[70:71], v[72:73]
	s_waitcnt vmcnt(25)
	v_lshlrev_b32_e32 v72, 16, v44
	v_and_b32_e32 v73, 0xffff0000, v44
	v_pk_add_f32 v[50:51], v[54:55], v[50:51]
	v_lshlrev_b32_e32 v44, 16, v45
	v_and_b32_e32 v45, 0xffff0000, v45
	v_pk_add_f32 v[70:71], v[70:71], v[72:73]
	s_waitcnt vmcnt(24)
	v_lshlrev_b32_e32 v72, 16, v42
	v_and_b32_e32 v73, 0xffff0000, v42
	v_pk_add_f32 v[44:45], v[50:51], v[44:45]
	v_lshlrev_b32_e32 v42, 16, v43
	v_and_b32_e32 v43, 0xffff0000, v43
	v_pk_add_f32 v[70:71], v[70:71], v[72:73]
	s_waitcnt vmcnt(23)
	v_lshlrev_b32_e32 v72, 16, v56
	v_and_b32_e32 v73, 0xffff0000, v56
	v_pk_add_f32 v[42:43], v[44:45], v[42:43]
	v_lshlrev_b32_e32 v44, 16, v57
	v_and_b32_e32 v45, 0xffff0000, v57
	v_pk_add_f32 v[70:71], v[70:71], v[72:73]
	s_waitcnt vmcnt(22)
	v_lshlrev_b32_e32 v72, 16, v58
	v_and_b32_e32 v73, 0xffff0000, v58
	v_pk_add_f32 v[42:43], v[42:43], v[44:45]
	v_lshlrev_b32_e32 v44, 16, v59
	v_and_b32_e32 v45, 0xffff0000, v59
	v_pk_add_f32 v[70:71], v[70:71], v[72:73]
	v_pk_add_f32 v[42:43], v[42:43], v[44:45]
	s_waitcnt vmcnt(21)
	v_lshlrev_b32_e32 v44, 16, v52
	v_and_b32_e32 v45, 0xffff0000, v52
	v_lshlrev_b32_e32 v50, 16, v53
	v_and_b32_e32 v51, 0xffff0000, v53
	s_waitcnt vmcnt(20)
	v_lshlrev_b32_e32 v52, 16, v48
	v_and_b32_e32 v53, 0xffff0000, v48
	v_lshlrev_b32_e32 v48, 16, v49
	v_and_b32_e32 v49, 0xffff0000, v49
	v_pk_add_f32 v[44:45], v[70:71], v[44:45]
	v_pk_add_f32 v[42:43], v[42:43], v[50:51]
	s_waitcnt vmcnt(19)
	v_lshlrev_b32_e32 v54, 16, v46
	v_and_b32_e32 v55, 0xffff0000, v46
	v_lshlrev_b32_e32 v46, 16, v47
	v_and_b32_e32 v47, 0xffff0000, v47
	v_pk_add_f32 v[44:45], v[44:45], v[52:53]
	v_pk_add_f32 v[42:43], v[42:43], v[48:49]
	v_pk_add_f32 v[44:45], v[44:45], v[54:55]
	s_waitcnt vmcnt(18)
	v_lshlrev_b32_e32 v52, 16, v30
	v_and_b32_e32 v53, 0xffff0000, v30
	v_pk_add_f32 v[42:43], v[42:43], v[46:47]
	v_lshlrev_b32_e32 v30, 16, v31
	v_and_b32_e32 v31, 0xffff0000, v31
	v_pk_add_f32 v[44:45], v[44:45], v[52:53]
	s_waitcnt vmcnt(17)
	v_lshlrev_b32_e32 v52, 16, v26
	v_and_b32_e32 v53, 0xffff0000, v26
	v_pk_add_f32 v[30:31], v[42:43], v[30:31]
	v_lshlrev_b32_e32 v26, 16, v27
	v_and_b32_e32 v27, 0xffff0000, v27
	v_pk_add_f32 v[44:45], v[44:45], v[52:53]
	s_waitcnt vmcnt(16)
	v_lshlrev_b32_e32 v52, 16, v22
	v_and_b32_e32 v53, 0xffff0000, v22
	v_pk_add_f32 v[26:27], v[30:31], v[26:27]
	v_lshlrev_b32_e32 v22, 16, v23
	v_and_b32_e32 v23, 0xffff0000, v23
	v_pk_add_f32 v[44:45], v[44:45], v[52:53]
	s_waitcnt vmcnt(15)
	v_lshlrev_b32_e32 v52, 16, v18
	v_and_b32_e32 v53, 0xffff0000, v18
	v_pk_add_f32 v[22:23], v[26:27], v[22:23]
	v_lshlrev_b32_e32 v18, 16, v19
	v_and_b32_e32 v19, 0xffff0000, v19
	v_pk_add_f32 v[44:45], v[44:45], v[52:53]
	s_waitcnt vmcnt(14)
	v_lshlrev_b32_e32 v52, 16, v16
	v_and_b32_e32 v53, 0xffff0000, v16
	v_pk_add_f32 v[18:19], v[22:23], v[18:19]
	v_lshlrev_b32_e32 v16, 16, v17
	v_and_b32_e32 v17, 0xffff0000, v17
	v_pk_add_f32 v[44:45], v[44:45], v[52:53]
	s_waitcnt vmcnt(13)
	v_lshlrev_b32_e32 v52, 16, v14
	v_and_b32_e32 v53, 0xffff0000, v14
	v_pk_add_f32 v[16:17], v[18:19], v[16:17]
	v_lshlrev_b32_e32 v14, 16, v15
	v_and_b32_e32 v15, 0xffff0000, v15
	v_pk_add_f32 v[44:45], v[44:45], v[52:53]
	s_waitcnt vmcnt(12)
	v_lshlrev_b32_e32 v52, 16, v12
	v_and_b32_e32 v53, 0xffff0000, v12
	v_pk_add_f32 v[14:15], v[16:17], v[14:15]
	v_lshlrev_b32_e32 v12, 16, v13
	v_and_b32_e32 v13, 0xffff0000, v13
	v_pk_add_f32 v[44:45], v[44:45], v[52:53]
	s_waitcnt vmcnt(11)
	v_lshlrev_b32_e32 v52, 16, v10
	v_and_b32_e32 v53, 0xffff0000, v10
	v_pk_add_f32 v[12:13], v[14:15], v[12:13]
	v_lshlrev_b32_e32 v10, 16, v11
	v_and_b32_e32 v11, 0xffff0000, v11
	v_pk_add_f32 v[44:45], v[44:45], v[52:53]
	v_pk_add_f32 v[10:11], v[12:13], v[10:11]
	s_waitcnt vmcnt(10)
	v_lshlrev_b32_e32 v12, 16, v8
	v_and_b32_e32 v13, 0xffff0000, v8
	v_lshlrev_b32_e32 v8, 16, v9
	v_and_b32_e32 v9, 0xffff0000, v9
	s_waitcnt vmcnt(9)
	v_lshlrev_b32_e32 v14, 16, v6
	v_and_b32_e32 v15, 0xffff0000, v6
	v_lshlrev_b32_e32 v6, 16, v7
	v_and_b32_e32 v7, 0xffff0000, v7
	s_waitcnt vmcnt(8)
	v_lshlrev_b32_e32 v16, 16, v4
	v_and_b32_e32 v17, 0xffff0000, v4
	v_lshlrev_b32_e32 v18, 16, v5
	v_and_b32_e32 v19, 0xffff0000, v5
	v_pk_add_f32 v[4:5], v[44:45], v[12:13]
	v_pk_add_f32 v[8:9], v[10:11], v[8:9]
	v_pk_add_f32 v[4:5], v[4:5], v[14:15]
	v_pk_add_f32 v[6:7], v[8:9], v[6:7]
	v_pk_add_f32 v[4:5], v[4:5], v[16:17]
	s_waitcnt vmcnt(7)
	v_lshlrev_b32_e32 v12, 16, v40
	v_and_b32_e32 v13, 0xffff0000, v40
	v_pk_add_f32 v[6:7], v[6:7], v[18:19]
	v_lshlrev_b32_e32 v8, 16, v41
	v_and_b32_e32 v9, 0xffff0000, v41
	v_pk_add_f32 v[4:5], v[4:5], v[12:13]
	s_waitcnt vmcnt(6)
	v_lshlrev_b32_e32 v12, 16, v38
	v_and_b32_e32 v13, 0xffff0000, v38
	v_pk_add_f32 v[6:7], v[6:7], v[8:9]
	v_lshlrev_b32_e32 v8, 16, v39
	v_and_b32_e32 v9, 0xffff0000, v39
	v_pk_add_f32 v[4:5], v[4:5], v[12:13]
	s_waitcnt vmcnt(5)
	v_lshlrev_b32_e32 v12, 16, v36
	v_and_b32_e32 v13, 0xffff0000, v36
	v_pk_add_f32 v[6:7], v[6:7], v[8:9]
	v_lshlrev_b32_e32 v8, 16, v37
	v_and_b32_e32 v9, 0xffff0000, v37
	v_pk_add_f32 v[4:5], v[4:5], v[12:13]
	s_waitcnt vmcnt(4)
	v_lshlrev_b32_e32 v12, 16, v34
	v_and_b32_e32 v13, 0xffff0000, v34
	v_pk_add_f32 v[6:7], v[6:7], v[8:9]
	v_lshlrev_b32_e32 v8, 16, v35
	v_and_b32_e32 v9, 0xffff0000, v35
	v_pk_add_f32 v[4:5], v[4:5], v[12:13]
	s_waitcnt vmcnt(3)
	v_lshlrev_b32_e32 v12, 16, v32
	v_and_b32_e32 v13, 0xffff0000, v32
	v_pk_add_f32 v[6:7], v[6:7], v[8:9]
	v_lshlrev_b32_e32 v8, 16, v33
	v_and_b32_e32 v9, 0xffff0000, v33
	v_pk_add_f32 v[4:5], v[4:5], v[12:13]
	s_waitcnt vmcnt(2)
	v_lshlrev_b32_e32 v12, 16, v28
	v_and_b32_e32 v13, 0xffff0000, v28
	v_pk_add_f32 v[6:7], v[6:7], v[8:9]
	v_lshlrev_b32_e32 v8, 16, v29
	v_and_b32_e32 v9, 0xffff0000, v29
	v_pk_add_f32 v[4:5], v[4:5], v[12:13]
	s_waitcnt vmcnt(1)
	v_lshlrev_b32_e32 v12, 16, v24
	v_and_b32_e32 v13, 0xffff0000, v24
	v_pk_add_f32 v[6:7], v[6:7], v[8:9]
	v_lshlrev_b32_e32 v8, 16, v25
	v_and_b32_e32 v9, 0xffff0000, v25
	v_pk_add_f32 v[4:5], v[4:5], v[12:13]
	s_waitcnt vmcnt(0)
	v_lshlrev_b32_e32 v12, 16, v20
	v_and_b32_e32 v13, 0xffff0000, v20
	v_pk_add_f32 v[6:7], v[6:7], v[8:9]
	v_lshlrev_b32_e32 v8, 16, v21
	v_and_b32_e32 v9, 0xffff0000, v21
	v_pk_add_f32 v[4:5], v[4:5], v[12:13]
	v_pk_add_f32 v[6:7], v[6:7], v[8:9]
	ds_write_b128 v2, v[4:7]
	s_waitcnt lgkmcnt(0)
	s_barrier
	s_and_saveexec_b64 s[0:1], vcc
	s_cbranch_execz .LBB0_625
	v_lshl_add_u32 v4, v64, 4, s65
	ds_read_b128 v[4:7], v4
	ds_read_b128 v[8:11], v2 offset:1024
	s_mov_b32 s4, 0x3b800000
	v_readlane_b32 s6, v255, 58
	v_lshlrev_b32_e32 v12, 2, v64
	s_waitcnt lgkmcnt(0)
	v_pk_add_f32 v[10:11], v[6:7], v[10:11]
	v_pk_add_f32 v[8:9], v[4:5], v[8:9]
	ds_read_b128 v[4:7], v2 offset:2048
	s_waitcnt lgkmcnt(0)
	v_pk_add_f32 v[10:11], v[10:11], v[6:7]
	v_pk_add_f32 v[8:9], v[8:9], v[4:5]
	ds_read_b128 v[4:7], v2 offset:3072
	s_waitcnt lgkmcnt(0)
	v_pk_add_f32 v[10:11], v[10:11], v[6:7]
	v_pk_add_f32 v[8:9], v[8:9], v[4:5]
	ds_read_b128 v[4:7], v2 offset:4096
	s_waitcnt lgkmcnt(0)
	v_pk_add_f32 v[10:11], v[10:11], v[6:7]
	v_pk_add_f32 v[8:9], v[8:9], v[4:5]
	ds_read_b128 v[4:7], v2 offset:5120
	s_waitcnt lgkmcnt(0)
	v_pk_add_f32 v[10:11], v[10:11], v[6:7]
	v_pk_add_f32 v[8:9], v[8:9], v[4:5]
	ds_read_b128 v[4:7], v2 offset:6144
	s_waitcnt lgkmcnt(0)
	v_pk_add_f32 v[10:11], v[10:11], v[6:7]
	v_pk_add_f32 v[8:9], v[8:9], v[4:5]
	ds_read_b128 v[4:7], v2 offset:7168
	v_lshlrev_b32_e32 v2, 2, v12
	s_waitcnt lgkmcnt(0)
	v_pk_add_f32 v[6:7], v[10:11], v[6:7]
	v_pk_add_f32 v[4:5], v[8:9], v[4:5]
	v_pk_mul_f32 v[6:7], v[6:7], s[4:5] op_sel_hi:[1,0]
	v_pk_mul_f32 v[4:5], v[4:5], s[4:5] op_sel_hi:[1,0]
	s_lshl_b64 s[4:5], s[48:49], 2
	s_add_u32 s4, s6, s4
	v_readlane_b32 s6, v255, 59
	s_addc_u32 s5, s6, s5
	global_store_dwordx4 v2, v[4:7], s[4:5]
